# loop-edge edit: dead hook tests removed from the peeled first K-iteration of the MoE loop (on v68)
# speedup vs baseline: 1.0027x; 1.0006x over previous
.Lpk_1899:
	s_mov_b64 s[0:1], 0
	s_mov_b64 s[52:53], 0
